# expert phase: 16 id reads and 8 partial reads batched before their consumers
# baseline (speedup 1.0000x reference)
; #define GAS __attribute__((address_space(1)))
; #define LAS __attribute__((address_space(3)))
; __device__ __forceinline__ void expert_phase(const Frame& F, int l, int xcc, LAS unsigned char* wl, const LAS unsigned char* zb) {
;     ...
;             unsigned suvq[8][2]; float gtq[8][2];
; #pragma unroll
;             for (int k = 0; k < 8; ++k)
; #pragma unroll
;                 for (int hf = 0; hf < 2; ++hf) { const unsigned e = *(const LAS unsigned short*)(IDL + k * 256 + (hf * 64 + lane) * 2);
;                     suvq[k][hf] = *(const GAS unsigned*)(SUV + e); gtq[k][hf] = *(const GAS float*)(GATE + (size_t)tok(k) * 128 + hf * 64 + lane); }
; #pragma unroll
;             for (int k = 0; k < 8; ++k) {
;                 float wq[2];
; #pragma unroll
;                 for (int hf = 0; hf < 2; ++hf) {
;                     const unsigned suv = suvq[k][hf];
;                     const int kk = hf * 64 + lane;
;                     const float a = (SA[k * 256 + (kk & 7) * 32 + (kk >> 3)] + SA[k * 256 + (kk & 7) * 32 + 16 + (kk >> 3)]) * bf_lo(suv);
;                     wq[hf] = gtq[k][hf] * bf_hi(suv) * 0.5f * a * (1.0f + erff(a * 0.7071067811865476f));
.LBB0_1159:
	s_waitcnt lgkmcnt(0)
	ds_read_u16 v226, v203 offset:10816
	ds_read_u16 v227, v206 offset:10816
	ds_read_u16 v228, v203 offset:11072
	ds_read_u16 v229, v206 offset:11072
	ds_read_u16 v230, v203 offset:11328
	ds_read_u16 v231, v206 offset:11328
	ds_read_u16 v232, v203 offset:11584
	ds_read_u16 v233, v206 offset:11584
	ds_read_u16 v234, v203 offset:11840
	ds_read_u16 v235, v206 offset:11840
	ds_read_u16 v236, v203 offset:12096
	ds_read_u16 v237, v206 offset:12096
	ds_read_u16 v238, v203 offset:12352
	ds_read_u16 v239, v206 offset:12352
	ds_read_u16 v240, v203 offset:12608
	ds_read_u16 v241, v206 offset:12608
	v_lshl_add_u64 v[0:1], v[160:161], 0, s[2:3]
	s_waitcnt vmcnt(21)
	v_lshl_add_u64 v[32:33], v[160:161], 0, s[44:45]
	s_waitcnt lgkmcnt(0)
	v_lshlrev_b32_e32 v2, 2, v226
	global_load_dword v30, v2, s[18:19]
	global_load_dword v31, v[0:1], off
	v_lshlrev_b32_e32 v2, 2, v227
	global_load_dword v12, v2, s[18:19]
	global_load_dword v29, v[0:1], off offset:256
	v_lshl_add_u64 v[0:1], v[160:161], 0, s[86:87]
	v_lshlrev_b32_e32 v2, 2, v228
	global_load_dword v27, v2, s[18:19]
	global_load_dword v28, v[0:1], off
	v_lshlrev_b32_e32 v2, 2, v229
	global_load_dword v25, v2, s[18:19]
	global_load_dword v26, v[0:1], off offset:256
	v_lshl_add_u64 v[0:1], v[160:161], 0, s[68:69]
	v_lshlrev_b32_e32 v2, 2, v230
	global_load_dword v23, v2, s[18:19]
	global_load_dword v24, v[0:1], off
	v_lshlrev_b32_e32 v2, 2, v231
	global_load_dword v21, v2, s[18:19]
	global_load_dword v22, v[0:1], off offset:256
	v_lshl_add_u64 v[0:1], v[160:161], 0, s[80:81]
	v_lshlrev_b32_e32 v2, 2, v232
	global_load_dword v19, v2, s[18:19]
	global_load_dword v20, v[0:1], off
	v_lshlrev_b32_e32 v2, 2, v233
	global_load_dword v17, v2, s[18:19]
	global_load_dword v18, v[0:1], off offset:256
	v_lshl_add_u64 v[0:1], v[160:161], 0, s[8:9]
	v_lshlrev_b32_e32 v2, 2, v234
	global_load_dword v15, v2, s[18:19]
	global_load_dword v16, v[0:1], off
	v_lshlrev_b32_e32 v2, 2, v235
	global_load_dword v13, v2, s[18:19]
	global_load_dword v14, v[0:1], off offset:256
	v_lshl_add_u64 v[0:1], v[160:161], 0, s[66:67]
	v_lshlrev_b32_e32 v2, 2, v236
	global_load_dword v10, v2, s[18:19]
	global_load_dword v11, v[0:1], off
	v_lshlrev_b32_e32 v2, 2, v237
	global_load_dword v8, v2, s[18:19]
	global_load_dword v9, v[0:1], off offset:256
	v_lshl_add_u64 v[0:1], v[160:161], 0, s[30:31]
	v_lshlrev_b32_e32 v2, 2, v238
	global_load_dword v4, v2, s[18:19]
	global_load_dword v5, v[0:1], off
	v_lshlrev_b32_e32 v2, 2, v239
	global_load_dword v2, v2, s[18:19]
	s_nop 0
	global_load_dword v3, v[0:1], off offset:256
	v_lshlrev_b32_e32 v0, 2, v240
	global_load_dword v0, v0, s[18:19]
	s_nop 0
	global_load_dword v1, v[32:33], off
	v_lshlrev_b32_e32 v6, 2, v241
	global_load_dword v6, v6, s[18:19]
	s_nop 0
	global_load_dword v7, v[32:33], off offset:256
	ds_read2_b32 v[32:33], v204 offset1:16
	s_waitcnt lgkmcnt(0)
	v_add_f32_e32 v32, v32, v33
	s_waitcnt vmcnt(31)
	v_lshlrev_b32_e32 v33, 16, v30
	v_mul_f32_e32 v32, v32, v33
	v_mul_f32_e32 v33, 0x3f3504f3, v32
	v_cmp_nlt_f32_e64 s[2:3], |v33|, 1.0
	s_and_saveexec_b64 s[4:5], s[2:3]
	s_xor_b64 s[2:3], exec, s[4:5]
	s_mov_b32 s10, 0xbfb8aa3b
	s_mov_b32 s11, 0x378e98ab
	s_mov_b32 s30, 0x3b7cd369
	s_mov_b32 s31, 0xbcc618b2
	s_mov_b32 s33, 0x3dda74e4
	s_mov_b32 s44, 0x3f228afd
	s_mov_b32 s45, 0x3e03c728
	s_mov_b32 s54, 0x42ce8ed0
	s_mov_b32 s55, 0xc2b17218
	s_cbranch_execz .LBB0_1161
	v_fma_f32 v34, |v33|, s11, v224
	v_fma_f32 v34, |v33|, v34, s30
	v_fma_f32 v34, |v33|, v34, s31
	v_fma_f32 v34, |v33|, v34, s33
	v_fma_f32 v34, |v33|, v34, s44
	v_fma_f32 v34, |v33|, v34, s45
	v_fma_f32 v34, |v33|, v34, |v33|
	v_mul_f32_e32 v35, 0xbfb8aa3b, v34
	v_fma_f32 v36, v34, s10, -v35
	v_rndne_f32_e32 v37, v35
	v_fmac_f32_e32 v36, 0xb2a5705f, v34
	v_sub_f32_e32 v35, v35, v37
	v_add_f32_e32 v35, v35, v36
	v_cvt_i32_f32_e32 v36, v37
	v_exp_f32_e32 v35, v35
	v_cmp_nlt_f32_e32 vcc, s54, v34
	v_ldexp_f32 v35, v35, v36
	s_nop 0
	v_cndmask_b32_e32 v35, 0, v35, vcc
	v_cmp_ngt_f32_e32 vcc, s55, v34
	s_nop 1
	v_cndmask_b32_e32 v34, v225, v35, vcc
	v_sub_f32_e32 v34, 1.0, v34

; #define GAS __attribute__((address_space(1)))
; __device__ __forceinline__ float frsq(float x) { return __builtin_amdgcn_rsqf(x); }
; __device__ __forceinline__ void expert_phase(const Frame& F, int l, int xcc, LAS unsigned char* wl, const LAS unsigned char* zb) {
;     ...
;         if (l + 1 < DEPTH) {
;             float* RSTD = (float*)(F.ws + WS_RSTD);
; #pragma unroll
;             for (int k = 0; k < 8; ++k) { const float r1 = frsq(wave_sum(SQ[k * 64 + lane]) * (1.f / D) + EPS); if (lane == 0) *(GAS float*)(RSTD + tok(k)) = r1; }
;         }
.LBB0_1249:
	s_waitcnt vmcnt(0)
	s_and_b64 vcc, exec, s[20:21]
	s_cbranch_vccz .LBB0_1124
	ds_read_b32 v226, v201 offset:8192
	ds_read_b32 v227, v201 offset:8448
	ds_read_b32 v228, v201 offset:8704
	ds_read_b32 v229, v201 offset:8960
	ds_read_b32 v230, v201 offset:9216
	ds_read_b32 v231, v201 offset:9472
	ds_read_b32 v232, v201 offset:9728
	ds_read_b32 v233, v201 offset:9984
	s_waitcnt lgkmcnt(0)
	v_mov_b32_e32 v0, v226
	s_waitcnt lgkmcnt(0)
	s_nop 1
	v_add_f32_dpp v0, v0, v0 quad_perm:[1,0,3,2] row_mask:0xf bank_mask:0xf
	s_nop 1
	v_add_f32_dpp v0, v0, v0 quad_perm:[2,3,0,1] row_mask:0xf bank_mask:0xf
	s_nop 1
	v_add_f32_dpp v0, v0, v0 row_half_mirror row_mask:0xf bank_mask:0xf
	s_nop 1
	v_add_f32_dpp v0, v0, v0 row_mirror row_mask:0xf bank_mask:0xf
	s_nop 1
	v_add_f32_dpp v0, v0, v0 row_bcast:15 row_mask:0xa bank_mask:0xf
	s_nop 1
	v_add_f32_dpp v0, v0, v0 row_bcast:31 row_mask:0xc bank_mask:0xf
	s_nop 1
	v_readlane_b32 s100, v0, 63
	s_nop 3
	v_mov_b32_e32 v0, s100
	v_mov_b32_e32 v1, 0
	s_and_saveexec_b64 s[2:3], s[34:35]
	s_cbranch_execz .LBB0_1252
	s_waitcnt lgkmcnt(0)
	v_add_f32_e32 v0, v0, v1
	v_fmamk_f32 v0, v0, 0x3a000000, v214
	v_rsq_f32_e32 v0, v0
	s_lshl_b64 s[4:5], s[26:27], 2
	v_readlane_b32 s8, v250, 22
	v_readlane_b32 s9, v250, 23
	s_add_u32 s4, s8, s4
	s_addc_u32 s5, s9, s5
	global_store_dword v185, v0, s[4:5]
.LBB0_1252:
	s_or_b64 exec, exec, s[2:3]
	v_mov_b32_e32 v0, v227
	s_waitcnt lgkmcnt(0)
	s_nop 1
	v_add_f32_dpp v0, v0, v0 quad_perm:[1,0,3,2] row_mask:0xf bank_mask:0xf
	s_nop 1
	v_add_f32_dpp v0, v0, v0 quad_perm:[2,3,0,1] row_mask:0xf bank_mask:0xf
	s_nop 1
	v_add_f32_dpp v0, v0, v0 row_half_mirror row_mask:0xf bank_mask:0xf
	s_nop 1
	v_add_f32_dpp v0, v0, v0 row_mirror row_mask:0xf bank_mask:0xf
	s_nop 1
	v_add_f32_dpp v0, v0, v0 row_bcast:15 row_mask:0xa bank_mask:0xf
	s_nop 1
	v_add_f32_dpp v0, v0, v0 row_bcast:31 row_mask:0xc bank_mask:0xf
	s_nop 1
	v_readlane_b32 s100, v0, 63
	s_nop 3
	v_mov_b32_e32 v0, s100
	v_mov_b32_e32 v1, 0
	s_and_saveexec_b64 s[2:3], s[34:35]
	s_cbranch_execz .LBB0_1254
	s_waitcnt lgkmcnt(0)
	v_add_f32_e32 v0, v0, v1
	v_fmamk_f32 v0, v0, 0x3a000000, v214
	v_rsq_f32_e32 v0, v0
	s_lshl_b64 s[4:5], s[88:89], 2
	v_readlane_b32 s8, v250, 22
	v_readlane_b32 s9, v250, 23
	s_add_u32 s4, s8, s4
	s_addc_u32 s5, s9, s5
	global_store_dword v185, v0, s[4:5]
.LBB0_1254:
	s_or_b64 exec, exec, s[2:3]
	v_mov_b32_e32 v0, v228
	s_waitcnt lgkmcnt(0)
	s_nop 1
	v_add_f32_dpp v0, v0, v0 quad_perm:[1,0,3,2] row_mask:0xf bank_mask:0xf
	s_nop 1
	v_add_f32_dpp v0, v0, v0 quad_perm:[2,3,0,1] row_mask:0xf bank_mask:0xf
	s_nop 1
	v_add_f32_dpp v0, v0, v0 row_half_mirror row_mask:0xf bank_mask:0xf
	s_nop 1
	v_add_f32_dpp v0, v0, v0 row_mirror row_mask:0xf bank_mask:0xf
	s_nop 1
	v_add_f32_dpp v0, v0, v0 row_bcast:15 row_mask:0xa bank_mask:0xf
	s_nop 1
	v_add_f32_dpp v0, v0, v0 row_bcast:31 row_mask:0xc bank_mask:0xf
	s_nop 1
	v_readlane_b32 s100, v0, 63
	s_nop 3
	v_mov_b32_e32 v0, s100
	v_mov_b32_e32 v1, 0
	s_and_saveexec_b64 s[2:3], s[34:35]
	s_cbranch_execz .LBB0_1256
	s_waitcnt lgkmcnt(0)
	v_add_f32_e32 v0, v0, v1
	v_fmamk_f32 v0, v0, 0x3a000000, v214
	v_rsq_f32_e32 v0, v0
	s_lshl_b64 s[0:1], s[0:1], 2
	v_readlane_b32 s4, v250, 22
	v_readlane_b32 s5, v250, 23
	s_add_u32 s0, s4, s0
	s_addc_u32 s1, s5, s1
	global_store_dword v185, v0, s[0:1]
.LBB0_1256:
	s_or_b64 exec, exec, s[2:3]
	v_mov_b32_e32 v0, v229
	s_waitcnt lgkmcnt(0)
	s_nop 1
	v_add_f32_dpp v0, v0, v0 quad_perm:[1,0,3,2] row_mask:0xf bank_mask:0xf
	s_nop 1
	v_add_f32_dpp v0, v0, v0 quad_perm:[2,3,0,1] row_mask:0xf bank_mask:0xf
	s_nop 1
	v_add_f32_dpp v0, v0, v0 row_half_mirror row_mask:0xf bank_mask:0xf
	s_nop 1
	v_add_f32_dpp v0, v0, v0 row_mirror row_mask:0xf bank_mask:0xf
	s_nop 1
	v_add_f32_dpp v0, v0, v0 row_bcast:15 row_mask:0xa bank_mask:0xf
	s_nop 1
	v_add_f32_dpp v0, v0, v0 row_bcast:31 row_mask:0xc bank_mask:0xf
	s_nop 1
	v_readlane_b32 s100, v0, 63
	s_nop 3
	v_mov_b32_e32 v0, s100
	v_mov_b32_e32 v1, 0
	s_and_saveexec_b64 s[0:1], s[34:35]
	s_cbranch_execz .LBB0_1258
	s_waitcnt lgkmcnt(0)
	v_add_f32_e32 v0, v0, v1
	v_fmamk_f32 v0, v0, 0x3a000000, v214
	v_rsq_f32_e32 v0, v0
	s_lshl_b64 s[2:3], s[16:17], 2
	v_readlane_b32 s4, v250, 22
	v_readlane_b32 s5, v250, 23
	s_add_u32 s2, s4, s2
	s_addc_u32 s3, s5, s3
	global_store_dword v185, v0, s[2:3]
; #define GAS __attribute__((address_space(1)))
; __device__ __forceinline__ float frsq(float x) { return __builtin_amdgcn_rsqf(x); }
; __device__ __forceinline__ void expert_phase(const Frame& F, int l, int xcc, LAS unsigned char* wl, const LAS unsigned char* zb) {
;     ...
;         if (l + 1 < DEPTH) {
;             float* RSTD = (float*)(F.ws + WS_RSTD);
; #pragma unroll
;             for (int k = 0; k < 8; ++k) { const float r1 = frsq(wave_sum(SQ[k * 64 + lane]) * (1.f / D) + EPS); if (lane == 0) *(GAS float*)(RSTD + tok(k)) = r1; }
;         }
.LBB0_1258:
	s_or_b64 exec, exec, s[0:1]
	v_mov_b32_e32 v0, v230
	s_waitcnt lgkmcnt(0)
	s_nop 1
	v_add_f32_dpp v0, v0, v0 quad_perm:[1,0,3,2] row_mask:0xf bank_mask:0xf
	s_nop 1
	v_add_f32_dpp v0, v0, v0 quad_perm:[2,3,0,1] row_mask:0xf bank_mask:0xf
	s_nop 1
	v_add_f32_dpp v0, v0, v0 row_half_mirror row_mask:0xf bank_mask:0xf
	s_nop 1
	v_add_f32_dpp v0, v0, v0 row_mirror row_mask:0xf bank_mask:0xf
	s_nop 1
	v_add_f32_dpp v0, v0, v0 row_bcast:15 row_mask:0xa bank_mask:0xf
	s_nop 1
	v_add_f32_dpp v0, v0, v0 row_bcast:31 row_mask:0xc bank_mask:0xf
	s_nop 1
	v_readlane_b32 s100, v0, 63
	s_nop 3
	v_mov_b32_e32 v0, s100
	v_mov_b32_e32 v1, 0
	s_and_saveexec_b64 s[0:1], s[34:35]
	s_cbranch_execz .LBB0_1260
	s_waitcnt lgkmcnt(0)
	v_add_f32_e32 v0, v0, v1
	v_fmamk_f32 v0, v0, 0x3a000000, v214
	v_rsq_f32_e32 v0, v0
	s_lshl_b64 s[2:3], s[14:15], 2
	v_readlane_b32 s4, v250, 22
	v_readlane_b32 s5, v250, 23
	s_add_u32 s2, s4, s2
	s_addc_u32 s3, s5, s3
	global_store_dword v185, v0, s[2:3]
.LBB0_1260:
	s_or_b64 exec, exec, s[0:1]
	v_mov_b32_e32 v0, v231
	s_waitcnt lgkmcnt(0)
	s_nop 1
	v_add_f32_dpp v0, v0, v0 quad_perm:[1,0,3,2] row_mask:0xf bank_mask:0xf
	s_nop 1
	v_add_f32_dpp v0, v0, v0 quad_perm:[2,3,0,1] row_mask:0xf bank_mask:0xf
	s_nop 1
	v_add_f32_dpp v0, v0, v0 row_half_mirror row_mask:0xf bank_mask:0xf
	s_nop 1
	v_add_f32_dpp v0, v0, v0 row_mirror row_mask:0xf bank_mask:0xf
	s_nop 1
	v_add_f32_dpp v0, v0, v0 row_bcast:15 row_mask:0xa bank_mask:0xf
	s_nop 1
	v_add_f32_dpp v0, v0, v0 row_bcast:31 row_mask:0xc bank_mask:0xf
	s_nop 1
	v_readlane_b32 s100, v0, 63
	s_nop 3
	v_mov_b32_e32 v0, s100
	v_mov_b32_e32 v1, 0
	s_and_saveexec_b64 s[0:1], s[34:35]
	s_cbranch_execz .LBB0_1262
	s_waitcnt lgkmcnt(0)
	v_add_f32_e32 v0, v0, v1
	v_fmamk_f32 v0, v0, 0x3a000000, v214
	v_rsq_f32_e32 v0, v0
	s_lshl_b64 s[2:3], s[12:13], 2
	v_readlane_b32 s4, v250, 22
	v_readlane_b32 s5, v250, 23
	s_add_u32 s2, s4, s2
	s_addc_u32 s3, s5, s3
	global_store_dword v185, v0, s[2:3]
.LBB0_1262:
	s_or_b64 exec, exec, s[0:1]
	v_mov_b32_e32 v0, v232
	s_waitcnt lgkmcnt(0)
	s_nop 1
	v_add_f32_dpp v0, v0, v0 quad_perm:[1,0,3,2] row_mask:0xf bank_mask:0xf
	s_nop 1
	v_add_f32_dpp v0, v0, v0 quad_perm:[2,3,0,1] row_mask:0xf bank_mask:0xf
	s_nop 1
	v_add_f32_dpp v0, v0, v0 row_half_mirror row_mask:0xf bank_mask:0xf
	s_nop 1
	v_add_f32_dpp v0, v0, v0 row_mirror row_mask:0xf bank_mask:0xf
	s_nop 1
	v_add_f32_dpp v0, v0, v0 row_bcast:15 row_mask:0xa bank_mask:0xf
	s_nop 1
	v_add_f32_dpp v0, v0, v0 row_bcast:31 row_mask:0xc bank_mask:0xf
	s_nop 1
	v_readlane_b32 s100, v0, 63
	s_nop 3
	v_mov_b32_e32 v0, s100
	v_mov_b32_e32 v1, 0
	s_and_saveexec_b64 s[0:1], s[34:35]
	s_cbranch_execz .LBB0_1264
	s_waitcnt lgkmcnt(0)
	v_add_f32_e32 v0, v0, v1
	v_fmamk_f32 v0, v0, 0x3a000000, v214
	v_rsq_f32_e32 v0, v0
	s_lshl_b64 s[2:3], s[94:95], 2
	v_readlane_b32 s4, v250, 22
	v_readlane_b32 s5, v250, 23
	s_add_u32 s2, s4, s2
	s_addc_u32 s3, s5, s3
	global_store_dword v185, v0, s[2:3]
.LBB0_1264:
	s_or_b64 exec, exec, s[0:1]
	v_mov_b32_e32 v0, v233
	s_waitcnt lgkmcnt(0)
	s_nop 1
	v_add_f32_dpp v0, v0, v0 quad_perm:[1,0,3,2] row_mask:0xf bank_mask:0xf
	s_nop 1
	v_add_f32_dpp v0, v0, v0 quad_perm:[2,3,0,1] row_mask:0xf bank_mask:0xf
	s_nop 1
	v_add_f32_dpp v0, v0, v0 row_half_mirror row_mask:0xf bank_mask:0xf
	s_nop 1
	v_add_f32_dpp v0, v0, v0 row_mirror row_mask:0xf bank_mask:0xf
	s_nop 1
	v_add_f32_dpp v0, v0, v0 row_bcast:15 row_mask:0xa bank_mask:0xf
	s_nop 1
	v_add_f32_dpp v0, v0, v0 row_bcast:31 row_mask:0xc bank_mask:0xf
	s_nop 1
	v_readlane_b32 s100, v0, 63
	s_nop 3
	v_mov_b32_e32 v0, s100
	v_mov_b32_e32 v1, 0
	s_and_saveexec_b64 s[0:1], s[34:35]
	s_cbranch_execz .LBB0_1123
	s_waitcnt lgkmcnt(0)
	v_add_f32_e32 v0, v0, v1
	v_fmamk_f32 v0, v0, 0x3a000000, v214
	v_rsq_f32_e32 v0, v0
	s_lshl_b64 s[2:3], s[6:7], 2
	v_readlane_b32 s4, v250, 22
	v_readlane_b32 s5, v250, 23
	s_add_u32 s2, s4, s2
	s_addc_u32 s3, s5, s3
	global_store_dword v185, v0, s[2:3]
	s_branch .LBB0_1123
